# LN1 router projection (f32 MFMA): operand loads double-buffered one K step ahead instead of load-wait per B tile
# speedup vs baseline: 1.0188x; 1.0188x over previous
.LBB0_3237:
	s_waitcnt vmcnt(0)
	s_add_i32 s10, s8, s9
	s_and_b32 s10, s10, 15
	s_lshl_b32 s64, s10, 6
	v_lshl_add_u64 v[76:77], v[32:33], 0, s[64:65]
	v_lshl_add_u64 v[78:79], v[34:35], 0, s[64:65]
	s_mul_i32 s64, s10, 0xc00
	v_lshl_add_u64 v[80:81], v[36:37], 0, s[64:65]
	global_load_dwordx4 v[56:59], v[76:77], off
	global_load_dwordx4 v[60:63], v[78:79], off
	global_load_dwordx4 v[88:91], v[80:81], off
	global_load_dwordx4 v[92:95], v[80:81], off offset:1024
	global_load_dwordx4 v[96:99], v[80:81], off offset:2048
.Lln1_rt_loop:
	s_add_i32 s10, s8, s9
	s_add_i32 s10, s10, 1
	s_and_b32 s10, s10, 15
	s_lshl_b32 s64, s10, 6
	v_lshl_add_u64 v[76:77], v[32:33], 0, s[64:65]
	v_lshl_add_u64 v[78:79], v[34:35], 0, s[64:65]
	s_mul_i32 s64, s10, 0xc00
	v_lshl_add_u64 v[80:81], v[36:37], 0, s[64:65]
	global_load_dwordx4 v[68:71], v[76:77], off
	global_load_dwordx4 v[72:75], v[78:79], off
	global_load_dwordx4 v[100:103], v[80:81], off
	global_load_dwordx4 v[104:107], v[80:81], off offset:1024
	global_load_dwordx4 v[108:111], v[80:81], off offset:2048
	s_waitcnt vmcnt(5)
	v_mfma_f32_16x16x4_f32 v[14:17], v56, v88, v[14:17]
	v_mfma_f32_16x16x4_f32 v[6:9], v60, v88, v[6:9]
	v_mfma_f32_16x16x4_f32 v[14:17], v57, v89, v[14:17]
	v_mfma_f32_16x16x4_f32 v[6:9], v61, v89, v[6:9]
	v_mfma_f32_16x16x4_f32 v[14:17], v58, v90, v[14:17]
	v_mfma_f32_16x16x4_f32 v[6:9], v62, v90, v[6:9]
	v_mfma_f32_16x16x4_f32 v[14:17], v59, v91, v[14:17]
	v_mfma_f32_16x16x4_f32 v[6:9], v63, v91, v[6:9]
	v_mfma_f32_16x16x4_f32 v[10:13], v56, v92, v[10:13]
	v_mfma_f32_16x16x4_f32 v[2:5], v60, v92, v[2:5]
	v_mfma_f32_16x16x4_f32 v[10:13], v57, v93, v[10:13]
	v_mfma_f32_16x16x4_f32 v[2:5], v61, v93, v[2:5]
	v_mfma_f32_16x16x4_f32 v[10:13], v58, v94, v[10:13]
	v_mfma_f32_16x16x4_f32 v[2:5], v62, v94, v[2:5]
	v_mfma_f32_16x16x4_f32 v[10:13], v59, v95, v[10:13]
	v_mfma_f32_16x16x4_f32 v[2:5], v63, v95, v[2:5]
	v_mfma_f32_16x16x4_f32 v[22:25], v56, v96, v[22:25]
	v_mfma_f32_16x16x4_f32 v[18:21], v60, v96, v[18:21]
	v_mfma_f32_16x16x4_f32 v[22:25], v57, v97, v[22:25]
	v_mfma_f32_16x16x4_f32 v[18:21], v61, v97, v[18:21]
	v_mfma_f32_16x16x4_f32 v[22:25], v58, v98, v[22:25]
	v_mfma_f32_16x16x4_f32 v[18:21], v62, v98, v[18:21]
	v_mfma_f32_16x16x4_f32 v[22:25], v59, v99, v[22:25]
	v_mfma_f32_16x16x4_f32 v[18:21], v63, v99, v[18:21]
	s_add_i32 s9, s9, 2
	s_cmp_lt_u32 s9, 16
	s_cbranch_scc0 .Lln1_rt_last
	s_add_i32 s10, s8, s9
	s_and_b32 s10, s10, 15
	s_lshl_b32 s64, s10, 6
	v_lshl_add_u64 v[76:77], v[32:33], 0, s[64:65]
	v_lshl_add_u64 v[78:79], v[34:35], 0, s[64:65]
	s_mul_i32 s64, s10, 0xc00
	v_lshl_add_u64 v[80:81], v[36:37], 0, s[64:65]
	global_load_dwordx4 v[56:59], v[76:77], off
	global_load_dwordx4 v[60:63], v[78:79], off
	global_load_dwordx4 v[88:91], v[80:81], off
	global_load_dwordx4 v[92:95], v[80:81], off offset:1024
	global_load_dwordx4 v[96:99], v[80:81], off offset:2048
	s_waitcnt vmcnt(5)
	v_mfma_f32_16x16x4_f32 v[14:17], v68, v100, v[14:17]
	v_mfma_f32_16x16x4_f32 v[6:9], v72, v100, v[6:9]
	v_mfma_f32_16x16x4_f32 v[14:17], v69, v101, v[14:17]
	v_mfma_f32_16x16x4_f32 v[6:9], v73, v101, v[6:9]
	v_mfma_f32_16x16x4_f32 v[14:17], v70, v102, v[14:17]
	v_mfma_f32_16x16x4_f32 v[6:9], v74, v102, v[6:9]
	v_mfma_f32_16x16x4_f32 v[14:17], v71, v103, v[14:17]
	v_mfma_f32_16x16x4_f32 v[6:9], v75, v103, v[6:9]
	v_mfma_f32_16x16x4_f32 v[10:13], v68, v104, v[10:13]
	v_mfma_f32_16x16x4_f32 v[2:5], v72, v104, v[2:5]
	v_mfma_f32_16x16x4_f32 v[10:13], v69, v105, v[10:13]
	v_mfma_f32_16x16x4_f32 v[2:5], v73, v105, v[2:5]
	v_mfma_f32_16x16x4_f32 v[10:13], v70, v106, v[10:13]
	v_mfma_f32_16x16x4_f32 v[2:5], v74, v106, v[2:5]
	v_mfma_f32_16x16x4_f32 v[10:13], v71, v107, v[10:13]
	v_mfma_f32_16x16x4_f32 v[2:5], v75, v107, v[2:5]
	v_mfma_f32_16x16x4_f32 v[22:25], v68, v108, v[22:25]
	v_mfma_f32_16x16x4_f32 v[18:21], v72, v108, v[18:21]
	v_mfma_f32_16x16x4_f32 v[22:25], v69, v109, v[22:25]
	v_mfma_f32_16x16x4_f32 v[18:21], v73, v109, v[18:21]
	v_mfma_f32_16x16x4_f32 v[22:25], v70, v110, v[22:25]
	v_mfma_f32_16x16x4_f32 v[18:21], v74, v110, v[18:21]
	v_mfma_f32_16x16x4_f32 v[22:25], v71, v111, v[22:25]
	v_mfma_f32_16x16x4_f32 v[18:21], v75, v111, v[18:21]
	s_branch .Lln1_rt_loop
.Lln1_rt_last:
	s_waitcnt vmcnt(0)
	v_mfma_f32_16x16x4_f32 v[14:17], v68, v100, v[14:17]
	v_mfma_f32_16x16x4_f32 v[6:9], v72, v100, v[6:9]
	v_mfma_f32_16x16x4_f32 v[14:17], v69, v101, v[14:17]
	v_mfma_f32_16x16x4_f32 v[6:9], v73, v101, v[6:9]
	v_mfma_f32_16x16x4_f32 v[14:17], v70, v102, v[14:17]
	v_mfma_f32_16x16x4_f32 v[6:9], v74, v102, v[6:9]
	v_mfma_f32_16x16x4_f32 v[14:17], v71, v103, v[14:17]
	v_mfma_f32_16x16x4_f32 v[6:9], v75, v103, v[6:9]
	v_mfma_f32_16x16x4_f32 v[10:13], v68, v104, v[10:13]
	v_mfma_f32_16x16x4_f32 v[2:5], v72, v104, v[2:5]
	v_mfma_f32_16x16x4_f32 v[10:13], v69, v105, v[10:13]
	v_mfma_f32_16x16x4_f32 v[2:5], v73, v105, v[2:5]
	v_mfma_f32_16x16x4_f32 v[10:13], v70, v106, v[10:13]
	v_mfma_f32_16x16x4_f32 v[2:5], v74, v106, v[2:5]
	v_mfma_f32_16x16x4_f32 v[10:13], v71, v107, v[10:13]
	v_mfma_f32_16x16x4_f32 v[2:5], v75, v107, v[2:5]
	v_mfma_f32_16x16x4_f32 v[22:25], v68, v108, v[22:25]
	v_mfma_f32_16x16x4_f32 v[18:21], v72, v108, v[18:21]
	v_mfma_f32_16x16x4_f32 v[22:25], v69, v109, v[22:25]
	v_mfma_f32_16x16x4_f32 v[18:21], v73, v109, v[18:21]
	v_mfma_f32_16x16x4_f32 v[22:25], v70, v110, v[22:25]
	v_mfma_f32_16x16x4_f32 v[18:21], v74, v110, v[18:21]
	v_mfma_f32_16x16x4_f32 v[22:25], v71, v111, v[22:25]
	v_mfma_f32_16x16x4_f32 v[18:21], v75, v111, v[18:21]


	s_setprio 0
	ds_write2_b32 v40, v14, v10 offset1:16
	ds_write2_b32 v40, v16, v12 offset0:96 offset1:112
	s_nop 4
	ds_write2_b32 v40, v22, v15 offset0:32 offset1:48
	ds_write2_b32 v40, v11, v23 offset0:64 offset1:80
	ds_write2_b32 v40, v24, v17 offset0:128 offset1:144
	ds_write2_b32 v40, v13, v25 offset0:160 offset1:176
	v_add_u32_e32 v10, 0xc00, v40
	ds_write2_b32 v10, v6, v2 offset1:16
	ds_write2_b32 v10, v8, v4 offset0:96 offset1:112
	ds_write2_b32 v10, v18, v7 offset0:32 offset1:48
	ds_write2_b32 v10, v3, v19 offset0:64 offset1:80
	ds_write2_b32 v10, v20, v9 offset0:128 offset1:144
	ds_write2_b32 v10, v5, v21 offset0:160 offset1:176
	s_waitcnt lgkmcnt(0)
	s_barrier
	s_and_saveexec_b64 s[8:9], s[6:7]
	s_cbranch_execz .LBB0_3241
	s_mov_b64 s[10:11], 0
	v_mov_b32_e32 v2, v39
	v_mov_b32_e32 v3, v66
